# ml_c prefetch wait ladder removed + MoE routing counters spread 256B apart (no same-line atomic serialisation)
# speedup vs baseline: 1.0234x; 1.0234x over previous
.LBB0_1070:
	s_waitcnt vmcnt(19)
	v_and_b32_e32 v248, 0xffff, v40
	s_waitcnt vmcnt(18)
	v_and_b32_e32 v249, 0xffff, v41
	s_waitcnt vmcnt(17)
	v_and_b32_e32 v250, 0xffff, v42
	s_waitcnt vmcnt(16)
	v_and_b32_e32 v172, 0xffff, v43
	s_waitcnt vmcnt(15)
	v_and_b32_e32 v174, 0xffff, v44
	s_waitcnt vmcnt(14)
	v_and_b32_e32 v175, 0xffff, v45
	s_waitcnt vmcnt(13)
	v_and_b32_e32 v176, 0xffff, v46
	s_waitcnt vmcnt(12)
	v_and_b32_e32 v177, 0xffff, v47
	s_waitcnt vmcnt(11)
	v_and_b32_e32 v178, 0xffff, v48
	s_waitcnt vmcnt(10)
	v_and_b32_e32 v179, 0xffff, v49
	s_waitcnt vmcnt(9)
	v_and_b32_e32 v180, 0xffff, v52
	s_waitcnt vmcnt(8)
	v_and_b32_e32 v181, 0xffff, v53
	s_waitcnt vmcnt(7)
	v_and_b32_e32 v182, 0xffff, v54
	s_waitcnt vmcnt(6)
	v_and_b32_e32 v183, 0xffff, v55
	s_waitcnt vmcnt(5)
	v_and_b32_e32 v184, 0xffff, v56
	s_waitcnt vmcnt(4)
	v_and_b32_e32 v185, 0xffff, v57
	s_mov_b32 s29, 1
	s_andn2_b64 vcc, exec, s[4:5]
	s_mul_i32 s52, s43, 0x1100
	s_cbranch_vccz .LBB0_1072
	s_branch .LBB0_1126

.LBB0_1080:
	ds_write_b128 v105, v[6:9]
	ds_write_b128 v105, v[2:5] offset:17408
	ds_write_b128 v106, v[14:17]
	ds_write_b128 v106, v[10:13] offset:17408
	ds_write_b16 v108, v248 offset:34816
	ds_write_b16 v109, v249 offset:34816
	ds_write_b16 v110, v250 offset:34816
	ds_write_b16 v112, v172 offset:34816
	ds_write_b16 v114, v174 offset:34816
	ds_write_b16 v116, v175 offset:34816
	ds_write_b16 v108, v176 offset:34864
	ds_write_b16 v119, v177 offset:34816
	ds_write_b16 v108, v178 offset:34880
	ds_write_b16 v122, v179 offset:34816
	ds_write_b16 v108, v180 offset:34896
	ds_write_b16 v125, v181 offset:34816
	ds_write_b16 v108, v182 offset:34912
	ds_write_b16 v128, v183 offset:34816
	ds_write_b16 v108, v184 offset:34928
	ds_write_b16 v131, v185 offset:34816
	ds_write_b128 v162, v[22:25] offset:55552
	ds_write_b128 v163, v[26:29] offset:55552
	ds_write_b128 v168, v[30:33] offset:55552
	s_and_saveexec_b64 s[46:47], s[14:15]
	ds_write_b128 v169, v[34:37] offset:55552
	s_or_b64 exec, exec, s[46:47]
	s_and_saveexec_b64 s[46:47], s[16:17]
	ds_write_b128 v170, v[18:21] offset:55552
	s_or_b64 exec, exec, s[46:47]
	s_mov_b32 s48, 0
	s_mov_b64 s[46:47], 0
	v_mov_b32_e32 v40, v0
	v_mov_b64_e32 v[38:39], v[0:1]
	s_branch .LBB0_1086

.LBB0_1090:
	s_or_b64 exec, exec, s[46:47]
	s_add_i32 s46, s24, s3
	s_cmpk_gt_i32 s46, 0x47f
	s_cselect_b64 s[48:49], -1, 0
	s_and_b64 vcc, exec, s[48:49]
	s_mov_b32 s50, s33
	v_mov_b32_e32 v186, v78
	s_waitcnt lgkmcnt(0)
	s_barrier
	s_cbranch_vccnz .LBB0_1098
	s_mul_hi_i32 s47, s46, 0x38e38e39
	s_lshr_b32 s50, s47, 31
	s_ashr_i32 s47, s47, 3
	s_add_i32 s47, s47, s50
	s_mul_i32 s50, s47, 36
	s_sub_i32 s50, s46, s50
	s_ashr_i32 s67, s47, 3
	s_bfe_u32 s63, s47, 0x20001
	s_and_b32 s64, s47, 1
	s_cmp_lt_i32 s50, 4
	s_cselect_b32 s47, 32, -4
	s_add_i32 s47, s47, s50
	s_sub_i32 s50, 35, s50
	s_cmp_eq_u32 s64, 0
	s_cselect_b32 s47, s47, s50
	s_lshl_b32 s65, s47, 6
	s_lshl_b32 s66, s67, 8
	s_addk_i32 s66, 0x1800
	s_lshl_b32 s67, s67, 11
	v_or_b32_e32 v2, s65, v218
	v_mov_b32_e32 v36, s66
	v_mov_b32_e32 v37, s67
	v_cmp_gt_i32_e32 vcc, s53, v2
	v_or_b32_e32 v12, s65, v85
	v_or_b32_e32 v18, s65, v107
	v_cndmask_b32_e32 v3, v36, v37, vcc
	v_cmp_gt_i32_e32 vcc, s53, v12
	v_or_b32_e32 v22, s65, v100
	v_or_b32_e32 v24, s65, v101
	v_cndmask_b32_e32 v13, v36, v37, vcc
	v_cmp_gt_i32_e32 vcc, s53, v18
	v_or_b32_e32 v26, s65, v111
	v_or_b32_e32 v28, s65, v113
	v_cndmask_b32_e32 v19, v36, v37, vcc
	v_cmp_gt_i32_e32 vcc, s53, v22
	v_or_b32_e32 v30, s65, v115
	v_or_b32_e32 v32, s65, v117
	v_cndmask_b32_e32 v23, v36, v37, vcc
	v_cmp_gt_i32_e32 vcc, s53, v24
	v_or_b32_e32 v34, s65, v118
	v_add_u32_e32 v20, v19, v18
	v_cndmask_b32_e32 v25, v36, v37, vcc
	v_cmp_gt_i32_e32 vcc, s53, v26
	v_mov_b64_e32 v[18:19], s[34:35]
	s_lshl_b32 s50, s63, 8
	v_cndmask_b32_e32 v27, v36, v37, vcc
	v_cmp_gt_i32_e32 vcc, s53, v28
	s_mov_b32 s51, s28
	v_mad_i64_i32 v[20:21], s[84:85], v20, s61, v[18:19]
	v_cndmask_b32_e32 v29, v36, v37, vcc
	v_cmp_gt_i32_e32 vcc, s53, v30
	v_add_u32_e32 v22, v23, v22
	v_add_u32_e32 v24, v25, v24
	v_cndmask_b32_e32 v31, v36, v37, vcc
	v_cmp_gt_i32_e32 vcc, s53, v32
	v_add_u32_e32 v26, v27, v26
	v_add_u32_e32 v28, v29, v28
	v_cndmask_b32_e32 v33, v36, v37, vcc
	v_cmp_gt_i32_e32 vcc, s53, v34
	v_add_u32_e32 v30, v31, v30
	v_add_u32_e32 v32, v33, v32
	v_cndmask_b32_e32 v35, v36, v37, vcc
	v_add_u32_e32 v34, v35, v34
	v_lshl_add_u64 v[10:11], v[80:81], 0, s[50:51]
	v_add_u32_e32 v2, v3, v2
	v_add_u32_e32 v12, v13, v12
	v_lshl_add_u64 v[20:21], v[20:21], 0, s[50:51]
	v_mov_b32_e32 v87, v79
	v_mad_i64_i32 v[22:23], s[84:85], v22, s61, v[18:19]
	v_mad_i64_i32 v[24:25], s[84:85], v24, s61, v[18:19]
	v_mad_i64_i32 v[26:27], s[84:85], v26, s61, v[18:19]
	v_mad_i64_i32 v[28:29], s[84:85], v28, s61, v[18:19]
	v_mad_i64_i32 v[30:31], s[84:85], v30, s61, v[18:19]
	v_mad_i64_i32 v[32:33], s[84:85], v32, s61, v[18:19]
	v_mad_i64_i32 v[34:35], s[84:85], v34, s61, v[18:19]
	v_mad_i64_i32 v[2:3], s[84:85], v2, s61, v[10:11]
	v_mad_i64_i32 v[10:11], s[84:85], v12, s61, v[10:11]
	v_lshl_add_u64 v[20:21], v[20:21], 0, v[86:87]
	v_lshl_add_u64 v[22:23], v[22:23], 0, s[50:51]
	v_lshl_add_u64 v[24:25], v[24:25], 0, s[50:51]
	v_lshl_add_u64 v[26:27], v[26:27], 0, s[50:51]
	v_lshl_add_u64 v[28:29], v[28:29], 0, s[50:51]
	v_lshl_add_u64 v[30:31], v[30:31], 0, s[50:51]
	v_lshl_add_u64 v[32:33], v[32:33], 0, s[50:51]
	v_lshl_add_u64 v[34:35], v[34:35], 0, s[50:51]
	global_load_dwordx4 v[6:9], v[2:3], off
	s_nop 0
	global_load_dwordx4 v[2:5], v[2:3], off offset:1024
	s_nop 0
	global_load_dwordx4 v[14:17], v[10:11], off
	s_nop 0
	global_load_dwordx4 v[10:13], v[10:11], off offset:1024
	v_lshl_add_u64 v[22:23], v[22:23], 0, v[86:87]
	v_lshl_add_u64 v[24:25], v[24:25], 0, v[86:87]
	v_lshl_add_u64 v[26:27], v[26:27], 0, v[86:87]
	v_lshl_add_u64 v[28:29], v[28:29], 0, v[86:87]
	v_lshl_add_u64 v[30:31], v[30:31], 0, v[86:87]
	v_lshl_add_u64 v[32:33], v[32:33], 0, v[86:87]
	v_lshl_add_u64 v[34:35], v[34:35], 0, v[86:87]
	global_load_ushort v248, v[20:21], off offset:2048
	global_load_ushort v249, v[22:23], off offset:2048
	global_load_ushort v250, v[24:25], off offset:2048
	global_load_ushort v172, v[26:27], off offset:2048
	global_load_ushort v174, v[28:29], off offset:2048
	global_load_ushort v175, v[30:31], off offset:2048
	global_load_ushort v176, v[32:33], off offset:2048
	global_load_ushort v177, v[34:35], off offset:2048
	v_or_b32_e32 v20, s65, v120
	v_cmp_gt_i32_e32 vcc, s53, v20
	v_or_b32_e32 v22, s65, v121
	v_or_b32_e32 v24, s65, v123
	v_cndmask_b32_e32 v21, v36, v37, vcc
	v_cmp_gt_i32_e32 vcc, s53, v22
	v_or_b32_e32 v26, s65, v124
	v_or_b32_e32 v28, s65, v126
	v_cndmask_b32_e32 v23, v36, v37, vcc
	v_cmp_gt_i32_e32 vcc, s53, v24
	v_or_b32_e32 v30, s65, v127
	v_or_b32_e32 v32, s65, v129
	v_cndmask_b32_e32 v25, v36, v37, vcc
	v_cmp_gt_i32_e32 vcc, s53, v26
	v_or_b32_e32 v34, s65, v130
	v_add_u32_e32 v20, v21, v20
	v_cndmask_b32_e32 v27, v36, v37, vcc
	v_cmp_gt_i32_e32 vcc, s53, v28
	v_mad_i64_i32 v[20:21], s[84:85], v20, s61, v[18:19]
	s_nop 0
	v_cndmask_b32_e32 v29, v36, v37, vcc
	v_cmp_gt_i32_e32 vcc, s53, v30
	v_add_u32_e32 v22, v23, v22
	v_add_u32_e32 v24, v25, v24
	v_cndmask_b32_e32 v31, v36, v37, vcc
	v_cmp_gt_i32_e32 vcc, s53, v32
	v_add_u32_e32 v26, v27, v26
	v_add_u32_e32 v28, v29, v28
	v_cndmask_b32_e32 v33, v36, v37, vcc
	v_cmp_gt_i32_e32 vcc, s53, v34
	v_add_u32_e32 v30, v31, v30
	v_add_u32_e32 v32, v33, v32
	v_cndmask_b32_e32 v35, v36, v37, vcc
	v_add_u32_e32 v34, v35, v34
	v_lshl_add_u64 v[20:21], v[20:21], 0, s[50:51]
	v_mad_i64_i32 v[22:23], s[84:85], v22, s61, v[18:19]
	v_mad_i64_i32 v[24:25], s[84:85], v24, s61, v[18:19]
	v_mad_i64_i32 v[26:27], s[84:85], v26, s61, v[18:19]
	v_mad_i64_i32 v[28:29], s[84:85], v28, s61, v[18:19]
	v_mad_i64_i32 v[30:31], s[84:85], v30, s61, v[18:19]
	v_mad_i64_i32 v[32:33], s[84:85], v32, s61, v[18:19]
	v_mad_i64_i32 v[18:19], s[84:85], v34, s61, v[18:19]
	v_lshl_add_u64 v[20:21], v[20:21], 0, v[86:87]
	v_lshl_add_u64 v[22:23], v[22:23], 0, s[50:51]
	v_lshl_add_u64 v[24:25], v[24:25], 0, s[50:51]
	v_lshl_add_u64 v[26:27], v[26:27], 0, s[50:51]
	v_lshl_add_u64 v[28:29], v[28:29], 0, s[50:51]
	v_lshl_add_u64 v[30:31], v[30:31], 0, s[50:51]
	v_lshl_add_u64 v[32:33], v[32:33], 0, s[50:51]
	v_lshl_add_u64 v[18:19], v[18:19], 0, s[50:51]
	v_lshl_add_u64 v[22:23], v[22:23], 0, v[86:87]
	v_lshl_add_u64 v[24:25], v[24:25], 0, v[86:87]
	v_lshl_add_u64 v[26:27], v[26:27], 0, v[86:87]
	v_lshl_add_u64 v[28:29], v[28:29], 0, v[86:87]
	v_lshl_add_u64 v[30:31], v[30:31], 0, v[86:87]
	v_lshl_add_u64 v[32:33], v[32:33], 0, v[86:87]
	v_lshl_add_u64 v[18:19], v[18:19], 0, v[86:87]
	global_load_ushort v178, v[20:21], off offset:2048
	global_load_ushort v179, v[22:23], off offset:2048
	global_load_ushort v180, v[24:25], off offset:2048
	global_load_ushort v181, v[26:27], off offset:2048
	global_load_ushort v182, v[28:29], off offset:2048
	global_load_ushort v183, v[30:31], off offset:2048
	global_load_ushort v184, v[32:33], off offset:2048
	global_load_ushort v185, v[18:19], off offset:2048
	v_mad_i64_i32 v[38:39], s[50:51], s46, v173, v[82:83]
	v_mov_b32_e32 v89, v79
	v_lshl_add_u64 v[18:19], v[38:39], 0, v[88:89]
	v_mov_b32_e32 v91, v79
	v_mov_b32_e32 v93, v79
	v_lshl_add_u64 v[20:21], v[38:39], 0, v[90:91]
	global_load_dwordx4 v[22:25], v[18:19], off
	global_load_dwordx4 v[26:29], v[20:21], off
	v_lshl_add_u64 v[18:19], v[38:39], 0, v[92:93]
	global_load_dwordx4 v[30:33], v[18:19], off
	v_mov_b32_e32 v20, v79
	v_mov_b32_e32 v21, v79
	v_mov_b32_e32 v18, 0
	v_mov_b32_e32 v19, v79
	v_mov_b64_e32 v[36:37], v[20:21]
	v_mov_b64_e32 v[34:35], v[18:19]
	s_and_saveexec_b64 s[50:51], s[18:19]
	s_cbranch_execz .LBB0_1093
	v_mov_b32_e32 v95, v79
	v_lshl_add_u64 v[34:35], v[38:39], 0, v[94:95]
	global_load_dwordx4 v[34:37], v[34:35], off

.LBB0_1097:
.LBB0_1098:
	s_cmp_gt_u32 s50, 15
	s_cbranch_scc1 .LBB0_1119
	s_and_b32 s47, s50, 3
	v_lshl_or_b32 v42, s47, 4, v84
	v_lshl_add_u32 v38, v42, 2, 0
	v_add_u32_e32 v38, 0x19600, v38
	s_lshr_b32 s63, s50, 2
	ds_read_b32 v43, v38
	s_mul_i32 s22, s63, 0x1100
	v_add_u32_e32 v44, s22, v159
	s_mul_i32 s22, s63, 0x900
	s_lshl_b32 s23, s47, 5
	s_or_b32 s22, s23, s22
	v_add_u32_e32 v46, s22, v160
	s_add_i32 s22, s50, -8
	v_lshl_or_b32 v45, s63, 4, v132
	v_lshl_or_b32 v47, s63, 6, v158
	v_mov_b32_e32 v48, s22
	s_branch .LBB0_1102

.LBB0_3223:
	s_waitcnt vmcnt(19)
	v_and_b32_e32 v248, 0xffff, v40
	s_waitcnt vmcnt(18)
	v_and_b32_e32 v249, 0xffff, v41
	s_waitcnt vmcnt(17)
	v_and_b32_e32 v250, 0xffff, v42
	s_waitcnt vmcnt(16)
	v_and_b32_e32 v173, 0xffff, v43
	s_waitcnt vmcnt(15)
	v_and_b32_e32 v174, 0xffff, v44
	s_waitcnt vmcnt(14)
	v_and_b32_e32 v175, 0xffff, v45
	s_waitcnt vmcnt(13)
	v_and_b32_e32 v176, 0xffff, v46
	s_waitcnt vmcnt(12)
	v_and_b32_e32 v177, 0xffff, v47
	s_waitcnt vmcnt(11)
	v_and_b32_e32 v178, 0xffff, v50
	s_waitcnt vmcnt(10)
	v_and_b32_e32 v179, 0xffff, v51
	s_waitcnt vmcnt(9)
	v_and_b32_e32 v180, 0xffff, v52
	s_waitcnt vmcnt(8)
	v_and_b32_e32 v181, 0xffff, v53
	s_waitcnt vmcnt(7)
	v_and_b32_e32 v182, 0xffff, v54
	s_waitcnt vmcnt(6)
	v_and_b32_e32 v183, 0xffff, v55
	s_waitcnt vmcnt(5)
	v_and_b32_e32 v184, 0xffff, v56
	s_waitcnt vmcnt(4)
	v_and_b32_e32 v185, 0xffff, v57
	s_branch .LBB0_3225

.LBB0_3234:
	ds_write_b128 v106, v[6:9]
	ds_write_b128 v106, v[2:5] offset:17408
	ds_write_b128 v107, v[14:17]
	ds_write_b128 v107, v[10:13] offset:17408
	ds_write_b16 v108, v248 offset:34816
	ds_write_b16 v109, v249 offset:34816
	ds_write_b16 v110, v250 offset:34816
	ds_write_b16 v112, v173 offset:34816
	ds_write_b16 v114, v174 offset:34816
	ds_write_b16 v116, v175 offset:34816
	ds_write_b16 v108, v176 offset:34864
	ds_write_b16 v119, v177 offset:34816
	ds_write_b16 v108, v178 offset:34880
	ds_write_b16 v122, v179 offset:34816
	ds_write_b16 v108, v180 offset:34896
	ds_write_b16 v125, v181 offset:34816
	ds_write_b16 v108, v182 offset:34912
	ds_write_b16 v128, v183 offset:34816
	ds_write_b16 v108, v184 offset:34928
	ds_write_b16 v131, v185 offset:34816
	ds_write_b128 v162, v[22:25] offset:55552
	ds_write_b128 v163, v[26:29] offset:55552
	ds_write_b128 v168, v[30:33] offset:55552
	s_and_saveexec_b64 s[46:47], s[14:15]
	ds_write_b128 v169, v[34:37] offset:55552
	s_or_b64 exec, exec, s[46:47]
	s_and_saveexec_b64 s[46:47], s[16:17]
	ds_write_b128 v170, v[18:21] offset:55552
	s_or_b64 exec, exec, s[46:47]
	s_mov_b32 s48, 0
	s_mov_b64 s[46:47], 0
	v_mov_b32_e32 v40, v0
	v_mov_b64_e32 v[38:39], v[0:1]
	s_branch .LBB0_3240

.LBB0_3244:
	s_or_b64 exec, exec, s[46:47]
	s_add_i32 s54, s45, s3
	s_cmpk_gt_i32 s54, 0x3ff
	s_cselect_b64 s[46:47], -1, 0
	s_and_b64 vcc, exec, s[46:47]
	s_mov_b32 s48, s33
	v_mov_b32_e32 v186, v78
	s_waitcnt lgkmcnt(0)
	s_barrier
	s_cbranch_vccnz .LBB0_3252
	s_ashr_i32 s48, s54, 31
	s_lshr_b32 s48, s48, 27
	s_add_i32 s49, s54, s48
	s_and_b32 s50, s49, 0xffffffe0
	s_ashr_i32 s48, s49, 5
	s_sub_i32 s50, s54, s50
	s_add_i32 s51, s50, 4
	s_bfe_u32 s55, s48, 0x20001
	s_and_b32 s69, s48, 1
	s_cmp_lt_i32 s50, 0
	s_cselect_b32 s70, 32, -4
	s_add_i32 s70, s70, s51
	s_sub_i32 s50, 31, s50
	s_cmp_eq_u32 s69, 0
	s_cselect_b32 s50, s70, s50
	s_lshl_b32 s70, s50, 6
	s_and_b32 s71, s49, 0xffffff00
	s_lshl_b32 s49, s49, 3
	s_addk_i32 s71, 0x1800
	s_and_b32 s72, s49, 0xfffff800
	v_or_b32_e32 v2, s70, v218
	v_mov_b32_e32 v36, s71
	v_mov_b32_e32 v37, s72
	v_cmp_gt_i32_e32 vcc, s58, v2
	v_or_b32_e32 v12, s70, v85
	v_or_b32_e32 v18, s70, v100
	v_cndmask_b32_e32 v3, v36, v37, vcc
	v_cmp_gt_i32_e32 vcc, s58, v12
	v_or_b32_e32 v22, s70, v101
	v_or_b32_e32 v24, s70, v102
	v_cndmask_b32_e32 v13, v36, v37, vcc
	v_cmp_gt_i32_e32 vcc, s58, v18
	v_or_b32_e32 v26, s70, v111
	v_or_b32_e32 v28, s70, v113
	v_cndmask_b32_e32 v19, v36, v37, vcc
	v_cmp_gt_i32_e32 vcc, s58, v22
	v_or_b32_e32 v30, s70, v115
	v_or_b32_e32 v32, s70, v117
	v_cndmask_b32_e32 v23, v36, v37, vcc
	v_cmp_gt_i32_e32 vcc, s58, v24
	v_or_b32_e32 v34, s70, v118
	s_mul_i32 s48, s48, 36
	v_cndmask_b32_e32 v25, v36, v37, vcc
	v_cmp_gt_i32_e32 vcc, s58, v26
	v_add_u32_e32 v20, v19, v18
	v_mov_b64_e32 v[18:19], s[30:31]
	v_cndmask_b32_e32 v27, v36, v37, vcc
	v_cmp_gt_i32_e32 vcc, s58, v28
	s_add_i32 s48, s48, s51
	s_lshl_b32 s50, s55, 8
	v_cndmask_b32_e32 v29, v36, v37, vcc
	v_cmp_gt_i32_e32 vcc, s58, v30
	s_mov_b32 s51, s24
	v_mad_i64_i32 v[20:21], s[84:85], v20, s66, v[18:19]
	v_cndmask_b32_e32 v31, v36, v37, vcc
	v_cmp_gt_i32_e32 vcc, s58, v32
	v_add_u32_e32 v22, v23, v22
	v_add_u32_e32 v24, v25, v24
	v_cndmask_b32_e32 v33, v36, v37, vcc
	v_cmp_gt_i32_e32 vcc, s58, v34
	v_add_u32_e32 v26, v27, v26
	v_add_u32_e32 v28, v29, v28
	v_cndmask_b32_e32 v35, v36, v37, vcc
	v_add_u32_e32 v30, v31, v30
	v_add_u32_e32 v32, v33, v32
	v_add_u32_e32 v34, v35, v34
	v_lshl_add_u64 v[10:11], v[80:81], 0, s[50:51]
	v_add_u32_e32 v2, v3, v2
	v_add_u32_e32 v12, v13, v12
	v_lshl_add_u64 v[20:21], v[20:21], 0, s[50:51]
	v_mov_b32_e32 v87, v79
	v_mad_i64_i32 v[22:23], s[84:85], v22, s66, v[18:19]
	v_mad_i64_i32 v[24:25], s[84:85], v24, s66, v[18:19]
	v_mad_i64_i32 v[26:27], s[84:85], v26, s66, v[18:19]
	v_mad_i64_i32 v[28:29], s[84:85], v28, s66, v[18:19]
	v_mad_i64_i32 v[30:31], s[84:85], v30, s66, v[18:19]
	v_mad_i64_i32 v[32:33], s[84:85], v32, s66, v[18:19]
	v_mad_i64_i32 v[34:35], s[84:85], v34, s66, v[18:19]
	v_mad_i64_i32 v[2:3], s[84:85], v2, s66, v[10:11]
	v_mad_i64_i32 v[10:11], s[84:85], v12, s66, v[10:11]
	v_lshl_add_u64 v[20:21], v[20:21], 0, v[86:87]
	v_lshl_add_u64 v[22:23], v[22:23], 0, s[50:51]
	v_lshl_add_u64 v[24:25], v[24:25], 0, s[50:51]
	v_lshl_add_u64 v[26:27], v[26:27], 0, s[50:51]
	v_lshl_add_u64 v[28:29], v[28:29], 0, s[50:51]
	v_lshl_add_u64 v[30:31], v[30:31], 0, s[50:51]
	v_lshl_add_u64 v[32:33], v[32:33], 0, s[50:51]
	v_lshl_add_u64 v[34:35], v[34:35], 0, s[50:51]
	global_load_dwordx4 v[6:9], v[2:3], off
	s_nop 0
	global_load_dwordx4 v[2:5], v[2:3], off offset:1024
	s_nop 0
	global_load_dwordx4 v[14:17], v[10:11], off
	s_nop 0
	global_load_dwordx4 v[10:13], v[10:11], off offset:1024
	v_lshl_add_u64 v[22:23], v[22:23], 0, v[86:87]
	v_lshl_add_u64 v[24:25], v[24:25], 0, v[86:87]
	v_lshl_add_u64 v[26:27], v[26:27], 0, v[86:87]
	v_lshl_add_u64 v[28:29], v[28:29], 0, v[86:87]
	v_lshl_add_u64 v[30:31], v[30:31], 0, v[86:87]
	v_lshl_add_u64 v[32:33], v[32:33], 0, v[86:87]
	v_lshl_add_u64 v[34:35], v[34:35], 0, v[86:87]
	global_load_ushort v248, v[20:21], off offset:2048
	global_load_ushort v249, v[22:23], off offset:2048
	global_load_ushort v250, v[24:25], off offset:2048
	global_load_ushort v173, v[26:27], off offset:2048
	global_load_ushort v174, v[28:29], off offset:2048
	global_load_ushort v175, v[30:31], off offset:2048
	global_load_ushort v176, v[32:33], off offset:2048
	global_load_ushort v177, v[34:35], off offset:2048
	v_or_b32_e32 v20, s70, v120
	v_cmp_gt_i32_e32 vcc, s58, v20
	v_or_b32_e32 v22, s70, v121
	v_or_b32_e32 v24, s70, v123
	v_cndmask_b32_e32 v21, v36, v37, vcc
	v_cmp_gt_i32_e32 vcc, s58, v22
	v_or_b32_e32 v26, s70, v124
	v_or_b32_e32 v28, s70, v126
	v_cndmask_b32_e32 v23, v36, v37, vcc
	v_cmp_gt_i32_e32 vcc, s58, v24
	v_or_b32_e32 v30, s70, v127
	v_or_b32_e32 v32, s70, v129
	v_cndmask_b32_e32 v25, v36, v37, vcc
	v_cmp_gt_i32_e32 vcc, s58, v26
	v_or_b32_e32 v34, s70, v130
	v_add_u32_e32 v20, v21, v20
	v_cndmask_b32_e32 v27, v36, v37, vcc
	v_cmp_gt_i32_e32 vcc, s58, v28
	v_mad_i64_i32 v[20:21], s[84:85], v20, s66, v[18:19]
	s_nop 0
	v_cndmask_b32_e32 v29, v36, v37, vcc
	v_cmp_gt_i32_e32 vcc, s58, v30
	v_add_u32_e32 v22, v23, v22
	v_add_u32_e32 v24, v25, v24
	v_cndmask_b32_e32 v31, v36, v37, vcc
	v_cmp_gt_i32_e32 vcc, s58, v32
	v_add_u32_e32 v26, v27, v26
	v_add_u32_e32 v28, v29, v28
	v_cndmask_b32_e32 v33, v36, v37, vcc
	v_cmp_gt_i32_e32 vcc, s58, v34
	v_add_u32_e32 v30, v31, v30
	v_add_u32_e32 v32, v33, v32
	v_cndmask_b32_e32 v35, v36, v37, vcc
	v_add_u32_e32 v34, v35, v34
	v_lshl_add_u64 v[20:21], v[20:21], 0, s[50:51]
	v_mad_i64_i32 v[22:23], s[84:85], v22, s66, v[18:19]
	v_mad_i64_i32 v[24:25], s[84:85], v24, s66, v[18:19]
	v_mad_i64_i32 v[26:27], s[84:85], v26, s66, v[18:19]
	v_mad_i64_i32 v[28:29], s[84:85], v28, s66, v[18:19]
	v_mad_i64_i32 v[30:31], s[84:85], v30, s66, v[18:19]
	v_mad_i64_i32 v[32:33], s[84:85], v32, s66, v[18:19]
	v_mad_i64_i32 v[18:19], s[84:85], v34, s66, v[18:19]
	v_lshl_add_u64 v[20:21], v[20:21], 0, v[86:87]
	v_lshl_add_u64 v[22:23], v[22:23], 0, s[50:51]
	v_lshl_add_u64 v[24:25], v[24:25], 0, s[50:51]
	v_lshl_add_u64 v[26:27], v[26:27], 0, s[50:51]
	v_lshl_add_u64 v[28:29], v[28:29], 0, s[50:51]
	v_lshl_add_u64 v[30:31], v[30:31], 0, s[50:51]
	v_lshl_add_u64 v[32:33], v[32:33], 0, s[50:51]
	v_lshl_add_u64 v[18:19], v[18:19], 0, s[50:51]
	v_lshl_add_u64 v[22:23], v[22:23], 0, v[86:87]
	v_lshl_add_u64 v[24:25], v[24:25], 0, v[86:87]
	v_lshl_add_u64 v[26:27], v[26:27], 0, v[86:87]
	v_lshl_add_u64 v[28:29], v[28:29], 0, v[86:87]
	v_lshl_add_u64 v[30:31], v[30:31], 0, v[86:87]
	v_lshl_add_u64 v[32:33], v[32:33], 0, v[86:87]
	v_lshl_add_u64 v[18:19], v[18:19], 0, v[86:87]
	global_load_ushort v178, v[20:21], off offset:2048
	global_load_ushort v179, v[22:23], off offset:2048
	global_load_ushort v180, v[24:25], off offset:2048
	global_load_ushort v181, v[26:27], off offset:2048
	global_load_ushort v182, v[28:29], off offset:2048
	global_load_ushort v183, v[30:31], off offset:2048
	global_load_ushort v184, v[32:33], off offset:2048
	global_load_ushort v185, v[18:19], off offset:2048
	v_mad_i64_i32 v[38:39], s[50:51], s48, v172, v[82:83]
	v_mov_b32_e32 v89, v79
	v_lshl_add_u64 v[18:19], v[38:39], 0, v[88:89]
	v_mov_b32_e32 v91, v79
	v_mov_b32_e32 v93, v79
	v_lshl_add_u64 v[20:21], v[38:39], 0, v[90:91]
	global_load_dwordx4 v[22:25], v[18:19], off
	global_load_dwordx4 v[26:29], v[20:21], off
	v_lshl_add_u64 v[18:19], v[38:39], 0, v[92:93]
	global_load_dwordx4 v[30:33], v[18:19], off
	v_mov_b32_e32 v20, v79
	v_mov_b32_e32 v21, v79
	v_mov_b32_e32 v18, 0
	v_mov_b32_e32 v19, v79
	v_mov_b64_e32 v[36:37], v[20:21]
	v_mov_b64_e32 v[34:35], v[18:19]
	s_and_saveexec_b64 s[50:51], s[18:19]
	s_cbranch_execz .LBB0_3247
	v_mov_b32_e32 v95, v79
	v_lshl_add_u64 v[34:35], v[38:39], 0, v[94:95]
	global_load_dwordx4 v[34:37], v[34:35], off

.LBB0_3251:
.LBB0_3252:
	s_cmp_gt_u32 s48, 15
	s_cbranch_scc1 .LBB0_3273
	s_and_b32 s50, s48, 3
	v_lshl_or_b32 v42, s50, 4, v84
	v_lshl_add_u32 v38, v42, 2, 0
	v_add_u32_e32 v38, 0x19600, v38
	s_lshr_b32 s51, s48, 2
	ds_read_b32 v43, v38
	s_mul_i32 s22, s51, 0x1100
	v_add_u32_e32 v44, s22, v159
	s_mul_i32 s22, s51, 0x900
	s_lshl_b32 s23, s50, 5
	s_or_b32 s22, s23, s22
	v_add_u32_e32 v46, s22, v160
	s_add_i32 s22, s48, -8
	v_lshl_or_b32 v45, s51, 4, v132
	v_lshl_or_b32 v47, s51, 6, v158
	v_mov_b32_e32 v48, s22
	s_branch .LBB0_3256

.LBB0_3684:
	s_mov_b64 s[8:9], exec
	v_mbcnt_lo_u32_b32 v36, s8, 0
	v_mbcnt_hi_u32_b32 v36, s9, v36
	v_cmp_eq_u32_e32 vcc, 0, v36
	s_and_saveexec_b64 s[6:7], vcc
	s_cbranch_execz .LBB0_3686
	s_lshl_b64 s[24:25], s[12:13], 8
	s_add_u32 s24, s36, s24
	s_addc_u32 s25, s37, s25
	s_bcnt1_i32_b64 s5, s[8:9]
	v_mov_b32_e32 v39, s5
	global_atomic_add v39, v123, v39, s[24:25] sc0
.LBB0_3686:
	s_or_b64 exec, exec, s[6:7]
	s_mov_b64 s[6:7], exec
	s_waitcnt vmcnt(0)
	v_readfirstlane_b32 s24, v39
	v_mbcnt_lo_u32_b32 v39, s6, 0
	v_mbcnt_hi_u32_b32 v39, s7, v39
	v_cmp_eq_u32_e32 vcc, 0, v39
	s_and_saveexec_b64 s[8:9], vcc
	s_cbranch_execz .LBB0_3677
	s_ashr_i32 s5, s4, 31
	s_lshl_b64 s[28:29], s[4:5], 8
	s_add_u32 s28, s36, s28
	s_addc_u32 s29, s37, s29
	s_bcnt1_i32_b64 s5, s[6:7]
	v_mov_b32_e32 v40, s5
	global_atomic_add v40, v123, v40, s[28:29] sc0
	s_branch .LBB0_3677

.LBB0_3887:
	s_cmp_gt_i32 s60, 27
	s_cselect_b64 s[0:1], -1, 0
	s_cmp_lt_i32 s61, 28
	s_cselect_b64 s[4:5], -1, 0
	s_or_b64 s[0:1], s[0:1], s[4:5]
	v_readlane_b32 s64, v247, 54
	s_and_b64 vcc, exec, s[0:1]
	v_readlane_b32 s70, v247, 60
	v_readlane_b32 s71, v247, 61
	s_mov_b64 s[72:73], s[60:61]
	v_readlane_b32 s65, v247, 55
	v_readlane_b32 s66, v247, 56
	v_readlane_b32 s67, v247, 57
	v_readlane_b32 s68, v247, 58
	v_readlane_b32 s69, v247, 59
	s_cbranch_vccnz .LBB0_3968
	s_barrier
	s_and_saveexec_b64 s[0:1], s[90:91]
	s_cbranch_execz .LBB0_3890
	s_waitcnt vmcnt(15)
	v_mov_b32_e32 v1, 0x10000
	global_load_dword v2, v1, s[26:27] sc1
	s_add_i32 s6, 0, 0x20040
	s_add_i32 s4, 0, 0x20000
	v_mov_b32_e32 v3, 0
	s_add_i32 s7, 0, 0x20080
	v_mov_b32_e32 v6, s6
	s_add_i32 s5, 0, 0x20020
	v_mov_b32_e32 v4, s4
	v_mov_b32_e32 v7, s7
	ds_write_b32 v6, v3
	ds_write_b32 v7, v3
	v_mov_b32_e32 v5, s5
	s_add_i32 s6, 0, 0x20044
	s_add_i32 s4, 0, 0x20004
	s_add_i32 s7, 0, 0x20084
	v_mov_b32_e32 v6, s6
	s_add_i32 s5, 0, 0x20024
	v_mov_b32_e32 v7, s7
	s_add_i32 s6, 0, 0x20048
	s_add_i32 s7, 0, 0x20088
	s_waitcnt vmcnt(0)
	v_add_u32_e32 v3, 0xff, v2
	ds_write_b32 v4, v2
	v_ashrrev_i32_e32 v2, 8, v3
	ds_write_b32 v5, v2
	global_load_dword v3, v1, s[26:27] offset:256 sc1
	v_mov_b32_e32 v4, s4
	v_mul_lo_u32 v8, v2, 56
	ds_write_b32 v6, v2
	ds_write_b32 v7, v8
	v_mov_b32_e32 v5, s5
	v_mov_b32_e32 v7, s6
	s_add_i32 s4, 0, 0x20008
	s_add_i32 s5, 0, 0x20028
	v_mov_b32_e32 v8, s7
	s_add_i32 s6, 0, 0x2004c
	s_add_i32 s7, 0, 0x2008c
	s_waitcnt vmcnt(0)
	v_add_u32_e32 v6, 0xff, v3
	ds_write_b32 v4, v3
	v_ashrrev_i32_e32 v3, 8, v6
	ds_write_b32 v5, v3
	global_load_dword v4, v1, s[26:27] offset:512 sc1
	v_add_u32_e32 v2, v3, v2
	v_mul_lo_u32 v3, v2, 56
	ds_write_b32 v7, v2
	ds_write_b32 v8, v3
	v_mov_b32_e32 v5, s4
	v_mov_b32_e32 v6, s5
	v_mov_b32_e32 v7, s6
	s_add_i32 s4, 0, 0x2000c
	s_add_i32 s5, 0, 0x2002c
	v_mov_b32_e32 v8, s7
	s_add_i32 s6, 0, 0x20050
	s_add_i32 s7, 0, 0x20090
	s_waitcnt vmcnt(0)
	v_add_u32_e32 v3, 0xff, v4
	v_ashrrev_i32_e32 v3, 8, v3
	ds_write_b32 v5, v4
	ds_write_b32 v6, v3
	global_load_dword v4, v1, s[26:27] offset:768 sc1
	v_add_u32_e32 v2, v3, v2
	v_mul_lo_u32 v3, v2, 56
	ds_write_b32 v7, v2
	ds_write_b32 v8, v3
	v_mov_b32_e32 v5, s4
	v_mov_b32_e32 v6, s5
	v_mov_b32_e32 v7, s6
	s_add_i32 s4, 0, 0x20010
	s_add_i32 s5, 0, 0x20030
	v_mov_b32_e32 v8, s7
	s_add_i32 s6, 0, 0x20054
	s_add_i32 s7, 0, 0x20094
	s_waitcnt vmcnt(0)
	v_add_u32_e32 v3, 0xff, v4
	v_ashrrev_i32_e32 v3, 8, v3
	ds_write_b32 v5, v4
	ds_write_b32 v6, v3
	global_load_dword v4, v1, s[26:27] offset:1024 sc1
	v_add_u32_e32 v2, v3, v2
	v_mul_lo_u32 v3, v2, 56
	ds_write_b32 v7, v2
	ds_write_b32 v8, v3
	v_mov_b32_e32 v5, s4
	v_mov_b32_e32 v6, s5
	v_mov_b32_e32 v7, s6
	s_add_i32 s4, 0, 0x20014
	s_add_i32 s5, 0, 0x20034
	v_mov_b32_e32 v8, s7
	s_add_i32 s6, 0, 0x20058
	s_add_i32 s7, 0, 0x20098
	s_waitcnt vmcnt(0)
	v_add_u32_e32 v3, 0xff, v4
	v_ashrrev_i32_e32 v3, 8, v3
	ds_write_b32 v5, v4
	ds_write_b32 v6, v3
	global_load_dword v4, v1, s[26:27] offset:1280 sc1
	v_add_u32_e32 v2, v3, v2
	v_mul_lo_u32 v3, v2, 56
	ds_write_b32 v7, v2
	ds_write_b32 v8, v3
	v_mov_b32_e32 v5, s4
	v_mov_b32_e32 v6, s5
	v_mov_b32_e32 v7, s6
	s_add_i32 s4, 0, 0x20018
	s_add_i32 s5, 0, 0x20038
	v_mov_b32_e32 v8, s7
	s_add_i32 s6, 0, 0x2005c
	s_add_i32 s7, 0, 0x2009c
	s_waitcnt vmcnt(0)
	v_add_u32_e32 v3, 0xff, v4
	v_ashrrev_i32_e32 v3, 8, v3
	ds_write_b32 v5, v4
	ds_write_b32 v6, v3
	global_load_dword v4, v1, s[26:27] offset:1536 sc1
	v_add_u32_e32 v2, v3, v2
	v_mul_lo_u32 v3, v2, 56
	ds_write_b32 v7, v2
	ds_write_b32 v8, v3
	v_mov_b32_e32 v5, s4
	v_mov_b32_e32 v6, s5
	s_add_i32 s4, 0, 0x2001c
	s_add_i32 s5, 0, 0x2003c
	s_waitcnt vmcnt(0)
	v_add_u32_e32 v3, 0xff, v4
	v_ashrrev_i32_e32 v3, 8, v3
	ds_write_b32 v5, v4
	ds_write_b32 v6, v3
	global_load_dword v1, v1, s[26:27] offset:1792 sc1
	v_mov_b32_e32 v4, s4
	v_mov_b32_e32 v5, s5
	v_add_u32_e32 v2, v3, v2
	v_mov_b32_e32 v6, s6
	v_mul_lo_u32 v3, v2, 56
	s_waitcnt vmcnt(0)
	v_add_u32_e32 v7, 0xff, v1
	ds_write_b32 v4, v1
	v_ashrrev_i32_e32 v1, 8, v7
	ds_write_b32 v5, v1
	v_add_u32_e32 v1, v1, v2
	v_mul_lo_u32 v4, v1, 56
	ds_write2_b32 v6, v2, v1 offset1:1
	v_mov_b32_e32 v1, s7
	ds_write2_b32 v1, v3, v4 offset1:1

.LBB0_3968:
	s_cmp_gt_i32 s72, 28
	s_cselect_b64 s[0:1], -1, 0
	s_cmp_lt_i32 s73, 29
	s_cselect_b64 s[4:5], -1, 0
	s_or_b64 s[0:1], s[0:1], s[4:5]
	s_and_b64 vcc, exec, s[0:1]
	s_cbranch_vccnz .LBB0_4084
	s_waitcnt vmcnt(0)
	s_barrier
	s_and_saveexec_b64 s[0:1], s[90:91]
	s_cbranch_execz .LBB0_3971
	v_mov_b32_e32 v1, 0x10000
	global_load_dword v2, v1, s[26:27] sc1
	s_add_i32 s6, 0, 0x20040
	s_add_i32 s4, 0, 0x20000
	v_mov_b32_e32 v3, 0
	s_add_i32 s7, 0, 0x20080
	v_mov_b32_e32 v6, s6
	s_add_i32 s5, 0, 0x20020
	v_mov_b32_e32 v4, s4
	v_mov_b32_e32 v7, s7
	ds_write_b32 v6, v3
	ds_write_b32 v7, v3
	v_mov_b32_e32 v5, s5
	s_add_i32 s6, 0, 0x20044
	s_add_i32 s4, 0, 0x20004
	s_add_i32 s7, 0, 0x20084
	v_mov_b32_e32 v6, s6
	s_add_i32 s5, 0, 0x20024
	v_mov_b32_e32 v7, s7
	s_add_i32 s6, 0, 0x20048
	s_add_i32 s7, 0, 0x20088
	s_waitcnt vmcnt(0)
	v_add_u32_e32 v3, 0xff, v2
	ds_write_b32 v4, v2
	v_ashrrev_i32_e32 v2, 8, v3
	ds_write_b32 v5, v2
	global_load_dword v3, v1, s[26:27] offset:256 sc1
	v_mov_b32_e32 v4, s4
	v_lshlrev_b32_e32 v8, 3, v2
	ds_write_b32 v6, v2
	ds_write_b32 v7, v8
	v_mov_b32_e32 v5, s5
	v_mov_b32_e32 v7, s6
	s_add_i32 s4, 0, 0x20008
	s_add_i32 s5, 0, 0x20028
	v_mov_b32_e32 v8, s7
	s_add_i32 s6, 0, 0x2004c
	s_add_i32 s7, 0, 0x2008c
	s_waitcnt vmcnt(0)
	v_add_u32_e32 v6, 0xff, v3
	ds_write_b32 v4, v3
	v_ashrrev_i32_e32 v3, 8, v6
	ds_write_b32 v5, v3
	global_load_dword v4, v1, s[26:27] offset:512 sc1
	v_add_u32_e32 v2, v3, v2
	v_lshlrev_b32_e32 v3, 3, v2
	ds_write_b32 v7, v2
	ds_write_b32 v8, v3
	v_mov_b32_e32 v5, s4
	v_mov_b32_e32 v6, s5
	v_mov_b32_e32 v7, s6
	s_add_i32 s4, 0, 0x2000c
	s_add_i32 s5, 0, 0x2002c
	v_mov_b32_e32 v8, s7
	s_add_i32 s6, 0, 0x20050
	s_add_i32 s7, 0, 0x20090
	s_waitcnt vmcnt(0)
	v_add_u32_e32 v3, 0xff, v4
	v_ashrrev_i32_e32 v3, 8, v3
	ds_write_b32 v5, v4
	ds_write_b32 v6, v3
	global_load_dword v4, v1, s[26:27] offset:768 sc1
	v_add_u32_e32 v2, v3, v2
	v_lshlrev_b32_e32 v3, 3, v2
	ds_write_b32 v7, v2
	ds_write_b32 v8, v3
	v_mov_b32_e32 v5, s4
	v_mov_b32_e32 v6, s5
	v_mov_b32_e32 v7, s6
	s_add_i32 s4, 0, 0x20010
	s_add_i32 s5, 0, 0x20030
	v_mov_b32_e32 v8, s7
	s_add_i32 s6, 0, 0x20054
	s_add_i32 s7, 0, 0x20094
	s_waitcnt vmcnt(0)
	v_add_u32_e32 v3, 0xff, v4
	v_ashrrev_i32_e32 v3, 8, v3
	ds_write_b32 v5, v4
	ds_write_b32 v6, v3
	global_load_dword v4, v1, s[26:27] offset:1024 sc1
	v_add_u32_e32 v2, v3, v2
	v_lshlrev_b32_e32 v3, 3, v2
	ds_write_b32 v7, v2
	ds_write_b32 v8, v3
	v_mov_b32_e32 v5, s4
	v_mov_b32_e32 v6, s5
	v_mov_b32_e32 v7, s6
	s_add_i32 s4, 0, 0x20014
	s_add_i32 s5, 0, 0x20034
	v_mov_b32_e32 v8, s7
	s_add_i32 s6, 0, 0x20058
	s_add_i32 s7, 0, 0x20098
	s_waitcnt vmcnt(0)
	v_add_u32_e32 v3, 0xff, v4
	v_ashrrev_i32_e32 v3, 8, v3
	ds_write_b32 v5, v4
	ds_write_b32 v6, v3
	global_load_dword v4, v1, s[26:27] offset:1280 sc1
	v_add_u32_e32 v2, v3, v2
	v_lshlrev_b32_e32 v3, 3, v2
	ds_write_b32 v7, v2
	ds_write_b32 v8, v3
	v_mov_b32_e32 v5, s4
	v_mov_b32_e32 v6, s5
	v_mov_b32_e32 v7, s6
	s_add_i32 s4, 0, 0x20018
	s_add_i32 s5, 0, 0x20038
	v_mov_b32_e32 v8, s7
	s_add_i32 s6, 0, 0x2005c
	s_add_i32 s7, 0, 0x2009c
	s_waitcnt vmcnt(0)
	v_add_u32_e32 v3, 0xff, v4
	v_ashrrev_i32_e32 v3, 8, v3
	ds_write_b32 v5, v4
	ds_write_b32 v6, v3
	global_load_dword v4, v1, s[26:27] offset:1536 sc1
	v_add_u32_e32 v2, v3, v2
	v_lshlrev_b32_e32 v3, 3, v2
	ds_write_b32 v7, v2
	ds_write_b32 v8, v3
	v_mov_b32_e32 v5, s4
	v_mov_b32_e32 v6, s5
	s_add_i32 s4, 0, 0x2001c
	s_add_i32 s5, 0, 0x2003c
	s_waitcnt vmcnt(0)
	v_add_u32_e32 v3, 0xff, v4
	v_ashrrev_i32_e32 v3, 8, v3
	ds_write_b32 v5, v4
	ds_write_b32 v6, v3
	global_load_dword v1, v1, s[26:27] offset:1792 sc1
	v_mov_b32_e32 v4, s4
	v_mov_b32_e32 v5, s5
	v_add_u32_e32 v2, v3, v2
	v_mov_b32_e32 v6, s6
	v_lshlrev_b32_e32 v3, 3, v2
	s_waitcnt vmcnt(0)
	v_add_u32_e32 v7, 0xff, v1
	ds_write_b32 v4, v1
	v_ashrrev_i32_e32 v1, 8, v7
	ds_write_b32 v5, v1
	v_add_u32_e32 v1, v1, v2
	v_lshlrev_b32_e32 v4, 3, v1
	ds_write2_b32 v6, v2, v1 offset1:1
	v_mov_b32_e32 v1, s7
	ds_write2_b32 v1, v3, v4 offset1:1

.LBB0_4084:
	s_cmp_gt_i32 s72, 29
	s_cselect_b64 s[0:1], -1, 0
	s_cmp_lt_i32 s73, 30
	s_cselect_b64 s[4:5], -1, 0
	s_or_b64 s[0:1], s[0:1], s[4:5]
	s_and_b64 vcc, exec, s[0:1]
	s_cbranch_vccnz .LBB0_4160
	s_waitcnt vmcnt(0)
	s_barrier
	s_and_saveexec_b64 s[0:1], s[90:91]
	s_cbranch_execz .LBB0_4087
	v_mov_b32_e32 v1, 0x10000
	global_load_dword v2, v1, s[26:27] sc1
	s_add_i32 s6, 0, 0x20040
	s_add_i32 s4, 0, 0x20000
	v_mov_b32_e32 v3, 0
	s_add_i32 s7, 0, 0x20080
	v_mov_b32_e32 v6, s6
	s_add_i32 s5, 0, 0x20020
	v_mov_b32_e32 v4, s4
	v_mov_b32_e32 v7, s7
	ds_write_b32 v6, v3
	ds_write_b32 v7, v3
	v_mov_b32_e32 v5, s5
	s_add_i32 s6, 0, 0x20044
	s_add_i32 s4, 0, 0x20004
	s_add_i32 s7, 0, 0x20084
	v_mov_b32_e32 v6, s6
	s_add_i32 s5, 0, 0x20024
	v_mov_b32_e32 v7, s7
	s_add_i32 s6, 0, 0x20048
	s_add_i32 s7, 0, 0x20088
	s_waitcnt vmcnt(0)
	v_add_u32_e32 v3, 0xff, v2
	ds_write_b32 v4, v2
	v_ashrrev_i32_e32 v2, 8, v3
	ds_write_b32 v5, v2
	global_load_dword v3, v1, s[26:27] offset:256 sc1
	v_mov_b32_e32 v4, s4
	v_lshlrev_b32_e32 v8, 3, v2
	ds_write_b32 v6, v2
	ds_write_b32 v7, v8
	v_mov_b32_e32 v5, s5
	v_mov_b32_e32 v7, s6
	s_add_i32 s4, 0, 0x20008
	s_add_i32 s5, 0, 0x20028
	v_mov_b32_e32 v8, s7
	s_add_i32 s6, 0, 0x2004c
	s_add_i32 s7, 0, 0x2008c
	s_waitcnt vmcnt(0)
	v_add_u32_e32 v6, 0xff, v3
	ds_write_b32 v4, v3
	v_ashrrev_i32_e32 v3, 8, v6
	ds_write_b32 v5, v3
	global_load_dword v4, v1, s[26:27] offset:512 sc1
	v_add_u32_e32 v2, v3, v2
	v_lshlrev_b32_e32 v3, 3, v2
	ds_write_b32 v7, v2
	ds_write_b32 v8, v3
	v_mov_b32_e32 v5, s4
	v_mov_b32_e32 v6, s5
	v_mov_b32_e32 v7, s6
	s_add_i32 s4, 0, 0x2000c
	s_add_i32 s5, 0, 0x2002c
	v_mov_b32_e32 v8, s7
	s_add_i32 s6, 0, 0x20050
	s_add_i32 s7, 0, 0x20090
	s_waitcnt vmcnt(0)
	v_add_u32_e32 v3, 0xff, v4
	v_ashrrev_i32_e32 v3, 8, v3
	ds_write_b32 v5, v4
	ds_write_b32 v6, v3
	global_load_dword v4, v1, s[26:27] offset:768 sc1
	v_add_u32_e32 v2, v3, v2
	v_lshlrev_b32_e32 v3, 3, v2
	ds_write_b32 v7, v2
	ds_write_b32 v8, v3
	v_mov_b32_e32 v5, s4
	v_mov_b32_e32 v6, s5
	v_mov_b32_e32 v7, s6
	s_add_i32 s4, 0, 0x20010
	s_add_i32 s5, 0, 0x20030
	v_mov_b32_e32 v8, s7
	s_add_i32 s6, 0, 0x20054
	s_add_i32 s7, 0, 0x20094
	s_waitcnt vmcnt(0)
	v_add_u32_e32 v3, 0xff, v4
	v_ashrrev_i32_e32 v3, 8, v3
	ds_write_b32 v5, v4
	ds_write_b32 v6, v3
	global_load_dword v4, v1, s[26:27] offset:1024 sc1
	v_add_u32_e32 v2, v3, v2
	v_lshlrev_b32_e32 v3, 3, v2
	ds_write_b32 v7, v2
	ds_write_b32 v8, v3
	v_mov_b32_e32 v5, s4
	v_mov_b32_e32 v6, s5
	v_mov_b32_e32 v7, s6
	s_add_i32 s4, 0, 0x20014
	s_add_i32 s5, 0, 0x20034
	v_mov_b32_e32 v8, s7
	s_add_i32 s6, 0, 0x20058
	s_add_i32 s7, 0, 0x20098
	s_waitcnt vmcnt(0)
	v_add_u32_e32 v3, 0xff, v4
	v_ashrrev_i32_e32 v3, 8, v3
	ds_write_b32 v5, v4
	ds_write_b32 v6, v3
	global_load_dword v4, v1, s[26:27] offset:1280 sc1
	v_add_u32_e32 v2, v3, v2
	v_lshlrev_b32_e32 v3, 3, v2
	ds_write_b32 v7, v2
	ds_write_b32 v8, v3
	v_mov_b32_e32 v5, s4
	v_mov_b32_e32 v6, s5
	v_mov_b32_e32 v7, s6
	s_add_i32 s4, 0, 0x20018
	s_add_i32 s5, 0, 0x20038
	v_mov_b32_e32 v8, s7
	s_add_i32 s6, 0, 0x2005c
	s_add_i32 s7, 0, 0x2009c
	s_waitcnt vmcnt(0)
	v_add_u32_e32 v3, 0xff, v4
	v_ashrrev_i32_e32 v3, 8, v3
	ds_write_b32 v5, v4
	ds_write_b32 v6, v3
	global_load_dword v4, v1, s[26:27] offset:1536 sc1
	v_add_u32_e32 v2, v3, v2
	v_lshlrev_b32_e32 v3, 3, v2
	ds_write_b32 v7, v2
	ds_write_b32 v8, v3
	v_mov_b32_e32 v5, s4
	v_mov_b32_e32 v6, s5
	s_add_i32 s4, 0, 0x2001c
	s_add_i32 s5, 0, 0x2003c
	s_waitcnt vmcnt(0)
	v_add_u32_e32 v3, 0xff, v4
	v_ashrrev_i32_e32 v3, 8, v3
	ds_write_b32 v5, v4
	ds_write_b32 v6, v3
	global_load_dword v1, v1, s[26:27] offset:1792 sc1
	v_mov_b32_e32 v4, s4
	v_mov_b32_e32 v5, s5
	v_add_u32_e32 v2, v3, v2
	v_mov_b32_e32 v6, s6
	v_lshlrev_b32_e32 v3, 3, v2
	s_waitcnt vmcnt(0)
	v_add_u32_e32 v7, 0xff, v1
	ds_write_b32 v4, v1
	v_ashrrev_i32_e32 v1, 8, v7
	ds_write_b32 v5, v1
	v_add_u32_e32 v1, v1, v2
	v_lshlrev_b32_e32 v4, 3, v1
	ds_write2_b32 v6, v2, v1 offset1:1
	v_mov_b32_e32 v1, s7
	ds_write2_b32 v1, v3, v4 offset1:1

.LBB0_4160:
	s_cmp_gt_i32 s72, 30
	s_cselect_b64 s[0:1], -1, 0
	s_cmp_lt_i32 s73, 31
	s_cselect_b64 s[4:5], -1, 0
	s_or_b64 s[0:1], s[0:1], s[4:5]
	s_and_b64 vcc, exec, s[0:1]
	s_cbranch_vccnz .LBB0_4167
	s_waitcnt vmcnt(0)
	s_barrier
	s_and_saveexec_b64 s[0:1], s[90:91]
	s_cbranch_execz .LBB0_4163
	v_mov_b32_e32 v0, 0x10000
	global_load_dword v1, v0, s[26:27] sc1
	v_mov_b32_e32 v2, 0
	ds_write_b32 v2, v2 offset:64
	ds_write_b32 v2, v2 offset:128
	s_waitcnt vmcnt(0)
	v_add_u32_e32 v3, 0xff, v1
	ds_write_b32 v2, v1
	v_ashrrev_i32_e32 v1, 8, v3
	ds_write_b32 v2, v1 offset:32
	global_load_dword v3, v0, s[26:27] offset:256 sc1
	ds_write_b32 v2, v1 offset:68
	ds_write_b32 v2, v1 offset:132
	s_waitcnt vmcnt(0)
	v_add_u32_e32 v4, 0xff, v3
	ds_write_b32 v2, v3 offset:4
	v_ashrrev_i32_e32 v3, 8, v4
	ds_write_b32 v2, v3 offset:36
	global_load_dword v4, v0, s[26:27] offset:512 sc1
	v_add_u32_e32 v1, v3, v1
	ds_write_b32 v2, v1 offset:72
	ds_write_b32 v2, v1 offset:136
	s_waitcnt vmcnt(0)
	v_add_u32_e32 v3, 0xff, v4
	v_ashrrev_i32_e32 v3, 8, v3
	ds_write_b32 v2, v4 offset:8
	ds_write_b32 v2, v3 offset:40
	global_load_dword v4, v0, s[26:27] offset:768 sc1
	v_add_u32_e32 v1, v3, v1
	ds_write_b32 v2, v1 offset:76
	ds_write_b32 v2, v1 offset:140
	s_waitcnt vmcnt(0)
	v_add_u32_e32 v3, 0xff, v4
	v_ashrrev_i32_e32 v3, 8, v3
	ds_write_b32 v2, v4 offset:12
	ds_write_b32 v2, v3 offset:44
	global_load_dword v4, v0, s[26:27] offset:1024 sc1
	v_add_u32_e32 v1, v3, v1
	ds_write_b32 v2, v1 offset:80
	ds_write_b32 v2, v1 offset:144
	s_waitcnt vmcnt(0)
	v_add_u32_e32 v3, 0xff, v4
	v_ashrrev_i32_e32 v3, 8, v3
	ds_write_b32 v2, v4 offset:16
	ds_write_b32 v2, v3 offset:48
	global_load_dword v4, v0, s[26:27] offset:1280 sc1
	v_add_u32_e32 v1, v3, v1
	ds_write_b32 v2, v1 offset:84
	ds_write_b32 v2, v1 offset:148
	s_waitcnt vmcnt(0)
	v_add_u32_e32 v3, 0xff, v4
	v_ashrrev_i32_e32 v3, 8, v3
	ds_write_b32 v2, v4 offset:20
	ds_write_b32 v2, v3 offset:52
	global_load_dword v4, v0, s[26:27] offset:1536 sc1
	v_add_u32_e32 v1, v3, v1
	ds_write_b32 v2, v1 offset:88
	ds_write_b32 v2, v1 offset:152
	s_waitcnt vmcnt(0)
	v_add_u32_e32 v3, 0xff, v4
	v_ashrrev_i32_e32 v3, 8, v3
	ds_write_b32 v2, v4 offset:24
	ds_write_b32 v2, v3 offset:56
	global_load_dword v0, v0, s[26:27] offset:1792 sc1
	v_add_u32_e32 v1, v3, v1
	s_waitcnt vmcnt(0)
	v_add_u32_e32 v3, 0xff, v0
	ds_write_b32 v2, v0 offset:28
	v_ashrrev_i32_e32 v0, 8, v3
	ds_write_b32 v2, v0 offset:60
	v_add_u32_e32 v0, v0, v1
	ds_write2_b32 v2, v1, v0 offset0:23 offset1:24
	ds_write2_b32 v2, v1, v0 offset0:39 offset1:40

	.amdhsa_kernel _Z10fwd_kernel4Args
		.amdhsa_group_segment_fixed_size 0
		.amdhsa_private_segment_fixed_size 0
		.amdhsa_kernarg_size 568
		.amdhsa_user_sgpr_count 2
		.amdhsa_user_sgpr_dispatch_ptr 0
		.amdhsa_user_sgpr_queue_ptr 0
		.amdhsa_user_sgpr_kernarg_segment_ptr 1
		.amdhsa_user_sgpr_dispatch_id 0
		.amdhsa_user_sgpr_kernarg_preload_length 0
		.amdhsa_user_sgpr_kernarg_preload_offset 0
		.amdhsa_user_sgpr_private_segment_size 0
		.amdhsa_uses_dynamic_stack 0
		.amdhsa_enable_private_segment 0
		.amdhsa_system_sgpr_workgroup_id_x 1
		.amdhsa_system_sgpr_workgroup_id_y 0
		.amdhsa_system_sgpr_workgroup_id_z 0
		.amdhsa_system_sgpr_workgroup_info 0
		.amdhsa_system_vgpr_workitem_id 0
		.amdhsa_next_free_vgpr 256
		.amdhsa_next_free_sgpr 98
		.amdhsa_accum_offset 256
		.amdhsa_reserve_vcc 1
		.amdhsa_float_round_mode_32 0
		.amdhsa_float_round_mode_16_64 0
		.amdhsa_float_denorm_mode_32 3
		.amdhsa_float_denorm_mode_16_64 3
		.amdhsa_dx10_clamp 1
		.amdhsa_ieee_mode 1
		.amdhsa_fp16_overflow 0
		.amdhsa_tg_split 0
		.amdhsa_exception_fp_ieee_invalid_op 0
		.amdhsa_exception_fp_denorm_src 0
		.amdhsa_exception_fp_ieee_div_zero 0
		.amdhsa_exception_fp_ieee_overflow 0
		.amdhsa_exception_fp_ieee_underflow 0
		.amdhsa_exception_fp_ieee_inexact 0
		.amdhsa_exception_int_div_zero 0
	.end_amdhsa_kernel

amdhsa.kernels:
  - .agpr_count:     0
    .args:
      - .offset:         0
        .size:           312
        .value_kind:     by_value
      - .offset:         312
        .size:           4
        .value_kind:     hidden_block_count_x
      - .offset:         316
        .size:           4
        .value_kind:     hidden_block_count_y
      - .offset:         320
        .size:           4
        .value_kind:     hidden_block_count_z
      - .offset:         324
        .size:           2
        .value_kind:     hidden_group_size_x
      - .offset:         326
        .size:           2
        .value_kind:     hidden_group_size_y
      - .offset:         328
        .size:           2
        .value_kind:     hidden_group_size_z
      - .offset:         330
        .size:           2
        .value_kind:     hidden_remainder_x
      - .offset:         332
        .size:           2
        .value_kind:     hidden_remainder_y
      - .offset:         334
        .size:           2
        .value_kind:     hidden_remainder_z
      - .offset:         352
        .size:           8
        .value_kind:     hidden_global_offset_x
      - .offset:         360
        .size:           8
        .value_kind:     hidden_global_offset_y
      - .offset:         368
        .size:           8
        .value_kind:     hidden_global_offset_z
      - .offset:         376
        .size:           2
        .value_kind:     hidden_grid_dims
      - .offset:         432
        .size:           4
        .value_kind:     hidden_dynamic_lds_size
    .group_segment_fixed_size: 0
    .kernarg_segment_align: 8
    .kernarg_segment_size: 568
    .language:       OpenCL C
    .language_version:
      - 2
      - 0
    .max_flat_workgroup_size: 512
    .name:           _Z10fwd_kernel4Args
    .private_segment_fixed_size: 0
    .sgpr_count:     104
    .sgpr_spill_count: 83
    .symbol:         _Z10fwd_kernel4Args.kd
    .uniform_work_group_size: 1
    .uses_dynamic_stack: false
    .vgpr_count:     256
    .vgpr_spill_count: 0
    .wavefront_size: 64
